# speedup vs baseline: 1.0034x; 1.0034x over previous
_Z15gemm_qkv_kernelPKDF16_S0_PDF16_S1_S1_PKfS3_S3_S3_S3_S1_PKiPyPj:
	s_load_dwordx8 s[36:43], s[0:1], 0x40
	s_load_dwordx4 s[28:31], s[0:1], 0x60
	s_mov_b64 s[4:5], -1
	s_cmpk_lt_i32 s2, 0x40
	s_movk_i32 s3, 0xc0
	s_cbranch_scc1 .LBB1_30
	s_add_i32 s2, s2, 0xffffffc0
	v_lshlrev_b32_e32 v1, 4, v0
	v_and_b32_e32 v2, 32, v0
	v_lshrrev_b32_e32 v4, 1, v0
	v_lshrrev_b32_e32 v5, 5, v0
	v_or_b32_e32 v13, 0x2000, v1
	s_load_dwordx16 s[12:27], s[0:1], 0x0
	v_bfe_u32 v12, v0, 2, 4
	v_bitop3_b32 v10, v1, v2, 48 bitop3:0x6c
	v_and_b32_e32 v4, 24, v4
	v_and_b32_e32 v5, 4, v5
	v_bfe_u32 v6, v0, 2, 2
	v_lshrrev_b32_e32 v1, 7, v13
	s_movk_i32 s0, 0x70
	s_ashr_i32 s33, s2, 31
	v_lshrrev_b32_e32 v3, 2, v0
	v_and_b32_e32 v11, 64, v0
	v_or3_b32 v4, v5, v6, v4
	v_and_or_b32 v1, v1, s0, v12
	s_lshr_b32 s0, s33, 29
	v_readfirstlane_b32 s1, v0
	v_or_b32_e32 v2, v10, v11
	v_and_or_b32 v3, v3, 64, v4
	s_add_i32 s0, s2, s0
	s_lshr_b32 s10, s1, 6
	v_lshl_or_b32 v164, v3, 12, v2
	v_lshrrev_b32_e32 v3, 6, v13
	s_ashr_i32 s4, s0, 3
	s_and_b32 s0, s0, -8
	v_and_or_b32 v3, v3, s3, v4
	s_lshr_b32 s44, s1, 8
	s_lshl_b32 s3, s10, 10
	s_sub_i32 s0, s2, s0
	s_cmp_lt_i32 s0, 0
	s_cselect_b32 s5, 25, 24
	s_mul_i32 s0, s0, s5
	s_add_i32 s0, s0, s4
	s_mul_hi_i32 s4, s0, 0x2aaaaaab
	s_lshr_b32 s5, s4, 31
	s_ashr_i32 s4, s4, 4
	s_add_i32 s4, s4, s5
	s_lshl_b32 s5, s4, 3
	s_mulk_i32 s4, 0x60
	s_sub_i32 s4, s0, s4
	s_bfe_i32 s0, s4, 0x80000
	s_bfe_u32 s0, s0, 0x3000c
	s_add_i32 s6, s4, s0
	s_bfe_i32 s0, s6, 0x80000
	s_and_b32 s6, s6, 0xf8
	s_sub_i32 s4, s4, s6
	s_sext_i32_i16 s0, s0
	s_sext_i32_i8 s4, s4
	s_lshr_b32 s0, s0, 3
	s_add_i32 s4, s5, s4
	s_and_b32 s5, s2, 7
	s_lshr_b32 s6, s2, 3
	s_lshr_b32 s4, s5, 1
	s_lshl_b32 s4, s4, 2
	s_and_b32 s0, s6, 3
	s_add_i32 s4, s4, s0
	s_and_b32 s0, s5, 1
	s_mul_i32 s0, s0, 6
	s_lshr_b32 s6, s6, 2
	s_add_i32 s0, s0, s6
	s_ashr_i32 s5, s4, 31
	s_bfe_i64 s[8:9], s[0:1], 0x100000
	s_lshl_b64 s[6:7], s[4:5], 20
	s_lshl_b64 s[8:9], s[8:9], 20
	s_waitcnt lgkmcnt(0)
	s_add_u32 s80, s20, 0x408000
	s_addc_u32 s81, s21, 0
	v_and_b32_e32 v241, 63, v0
	v_lshlrev_b32_e32 v241, 2, v241
	s_add_u32 s8, s14, s8
	s_addc_u32 s9, s15, s9
	s_add_i32 s58, s3, 0
	s_add_i32 m0, s58, 0x10000
	v_lshl_or_b32 v168, v3, 12, v2
	global_load_lds_dwordx4 v164, s[8:9]
	s_add_i32 m0, s58, 0x12000
	s_add_u32 s34, s8, 0x20000
	global_load_lds_dwordx4 v168, s[8:9]
	s_addc_u32 s35, s9, 0
	s_add_i32 m0, s58, 0x14000
	v_lshrrev_b32_e32 v5, 3, v0
	global_load_lds_dwordx4 v164, s[34:35]
	s_add_i32 m0, s58, 0x16000
	s_add_u32 s6, s12, s6
	v_and_or_b32 v5, v5, 48, v12
	s_addc_u32 s7, s13, s7
	s_add_i32 s59, s58, 0x2000
	v_lshl_or_b32 v162, v5, 12, v2
	global_load_lds_dwordx4 v168, s[34:35]
	s_mov_b32 m0, s58
	s_add_u32 s34, s6, 0x80000
	v_lshl_or_b32 v166, v1, 12, v2
	global_load_lds_dwordx4 v162, s[6:7]
	s_mov_b32 m0, s59
	s_addc_u32 s35, s7, 0
	s_add_i32 s60, s58, 0x4000
	global_load_lds_dwordx4 v166, s[6:7]
	s_mov_b32 m0, s60
	s_add_i32 s61, s58, 0x6000
	global_load_lds_dwordx4 v162, s[34:35]
	s_mov_b32 m0, s61
	v_mov_b32_e32 v171, 0
	global_load_lds_dwordx4 v166, s[34:35]
	v_mov_b32_e32 v165, v171
	v_mov_b32_e32 v169, v171
	v_mov_b32_e32 v163, v171
	v_mov_b32_e32 v167, v171
	s_cmp_eq_u32 s44, 1
	s_mov_b32 s11, 0
	v_lshl_add_u64 v[8:9], s[8:9], 0, v[164:165]
	v_lshl_add_u64 v[6:7], s[8:9], 0, v[168:169]
	v_lshl_add_u64 v[2:3], s[6:7], 0, v[162:163]
	s_cselect_b64 s[34:35], -1, 0
	s_cmp_lg_u32 s44, 1
	v_lshl_add_u64 v[4:5], s[6:7], 0, v[166:167]
	s_cbranch_scc1 .LBB1_3
	s_barrier
